# post-projection per-token loop: the indexer-q and k rope loads also issued at the top of the iteration (one load burst per token instead of three dependent groups)
# baseline (speedup 1.0000x reference)
.LBB0_325:
	global_load_dword v36, v195, s[0:1]
	v_lshl_add_u64 v[34:35], s[50:51], 0, v[26:27]
	global_load_ushort v37, v[34:35], off offset:-1024
	global_load_ushort v40, v[34:35], off offset:-992
	global_load_ushort v42, v[34:35], off
	global_load_ushort v43, v[34:35], off offset:32
	v_lshl_add_u64 v[38:39], s[50:51], 0, v[24:25]
	global_load_ushort v250, v[38:39], off offset:-1024
	global_load_ushort v251, v[38:39], off offset:-1008
	global_load_ushort v252, v[38:39], off
	global_load_ushort v253, v[38:39], off offset:16
	s_mov_b32 s98, 0x37cd0000
	s_mov_b32 s99, 0
	v_lshl_add_u64 v[244:245], s[50:51], 0, v[16:17]
	v_lshl_add_u64 v[244:245], v[244:245], 0, s[98:99]
	s_mov_b64 s[96:97], exec
	s_and_b64 exec, exec, s[6:7]
	global_load_ushort v254, v[244:245], off offset:2048
	global_load_ushort v255, v[244:245], off offset:2080
	s_mov_b64 exec, s[96:97]
	s_waitcnt vmcnt(9)
	v_lshlrev_b32_e32 v45, 16, v37
	v_cvt_f32_i32_e32 v44, v36
	s_waitcnt vmcnt(8)
	v_lshlrev_b32_e32 v46, 16, v40
	v_mul_f32_e32 v36, v1, v44
	v_cvt_f64_f32_e32 v[36:37], v36
	v_mul_f64 v[40:41], v[36:37], s[62:63]
	v_rndne_f64_e32 v[40:41], v[40:41]
	v_fmac_f64_e32 v[36:37], s[70:71], v[40:41]
	v_cvt_f32_f64_e32 v36, v[36:37]
	v_mul_f32_e32 v37, 0.15915494, v36
	v_sin_f32_e32 v36, v37
	v_cos_f32_e32 v37, v37
	s_waitcnt vmcnt(7)
	v_lshlrev_b32_e32 v40, 16, v42
	s_waitcnt vmcnt(6)
	v_lshlrev_b32_e32 v41, 16, v43
	v_mul_f32_e32 v42, v36, v46
	v_mul_f32_e32 v43, v37, v46
	v_mul_f32_e32 v46, v36, v41
	v_mul_f32_e32 v41, v37, v41
	v_fma_f32 v42, v37, v45, -v42
	v_fmac_f32_e32 v43, v36, v45
	v_fma_f32 v45, v37, v40, -v46
	v_fmac_f32_e32 v41, v36, v40
	v_bfe_u32 v40, v42, 16, 1
	v_bfe_u32 v46, v43, 16, 1
	v_bfe_u32 v47, v45, 16, 1
	v_bfe_u32 v48, v41, 16, 1
	v_add3_u32 v40, v42, v40, s3
	v_add3_u32 v42, v43, v46, s3
	v_add3_u32 v43, v45, v47, s3
	v_add3_u32 v41, v41, v48, s3
	global_store_short_d16_hi v[34:35], v40, off offset:-1024
	global_store_short_d16_hi v[34:35], v42, off offset:-992
	global_store_short_d16_hi v[34:35], v43, off
	global_store_short_d16_hi v[34:35], v41, off offset:32
	s_nop 0
	v_mul_f32_e32 v34, v28, v44
	v_cvt_f64_f32_e32 v[34:35], v34
	v_mul_f64 v[40:41], v[34:35], s[62:63]
	v_rndne_f64_e32 v[40:41], v[40:41]
	v_fmac_f64_e32 v[34:35], s[70:71], v[40:41]
	v_cvt_f32_f64_e32 v34, v[34:35]
	v_mul_f32_e32 v35, 0.15915494, v34
	v_sin_f32_e32 v34, v35
	v_cos_f32_e32 v35, v35
	s_waitcnt vmcnt(6)
	v_lshlrev_b32_e32 v40, 16, v250
	v_lshlrev_b32_e32 v41, 16, v251
	v_mul_f32_e32 v44, v34, v41
	v_lshlrev_b32_e32 v43, 16, v253
	v_lshlrev_b32_e32 v42, 16, v252
	v_mul_f32_e32 v41, v35, v41
	v_mul_f32_e32 v45, v34, v43
	v_mul_f32_e32 v43, v35, v43
	v_fma_f32 v44, v35, v40, -v44
	v_fmac_f32_e32 v41, v34, v40
	v_fma_f32 v40, v35, v42, -v45
	v_fmac_f32_e32 v43, v34, v42
	v_bfe_u32 v42, v44, 16, 1
	v_bfe_u32 v45, v41, 16, 1
	v_bfe_u32 v46, v40, 16, 1
	v_bfe_u32 v47, v43, 16, 1
	v_add3_u32 v42, v44, v42, s3
	v_add3_u32 v41, v41, v45, s3
	v_add3_u32 v40, v40, v46, s3
	v_add3_u32 v43, v43, v47, s3
	global_store_short_d16_hi v[38:39], v42, off offset:-1024
	global_store_short_d16_hi v[38:39], v41, off offset:-1008
	global_store_short_d16_hi v[38:39], v40, off
	global_store_short_d16_hi v[38:39], v43, off offset:16
	s_and_saveexec_b64 s[72:73], s[6:7]
	s_cbranch_execz .LBB0_324
	v_lshl_add_u64 v[38:39], s[50:51], 0, v[16:17]
	v_add_co_u32_e32 v38, vcc, 0x37cd0000, v38
	v_mov_b32_e32 v42, 0
	s_nop 0
	v_addc_co_u32_e32 v39, vcc, 0, v39, vcc
	v_mov_b32_e32 v43, 0
	v_lshl_add_u64 v[38:39], s[50:51], 0, v[6:7]
	v_add_co_u32_e32 v38, vcc, 0x4d6d0000, v38
	s_waitcnt vmcnt(8)
	v_lshlrev_b32_e32 v40, 16, v254
	v_lshlrev_b32_e32 v41, 16, v255
	v_mul_f32_e32 v44, v36, v41
	v_mul_f32_e32 v41, v37, v41
	v_fma_f32 v37, v37, v40, -v44
	v_fmac_f32_e32 v41, v36, v40
	v_cvt_pk_fp8_f32 v42, v37, v37
	v_cvt_pk_fp8_f32 v43, v41, v41
	v_addc_co_u32_e32 v39, vcc, 0, v39, vcc
	global_store_byte v[38:39], v42, off
	global_store_byte v[38:39], v43, off offset:16
	s_branch .LBB0_324
